# rope-path cs prefetch as before plus 212 bytes of s_nop in a once-per-WG block so every later K-loop keeps the byte alignment it had in the previous best version
# speedup vs baseline: 1.0020x; 1.0020x over previous
.LBB0_491:
	s_nop 0
	s_nop 0
	s_nop 0
	s_nop 0
	s_nop 0
	s_nop 0
	s_nop 0
	s_nop 0
	s_nop 0
	s_nop 0
	s_nop 0
	s_nop 0
	s_nop 0
	s_nop 0
	s_nop 0
	s_nop 0
	s_nop 0
	s_nop 0
	s_nop 0
	s_nop 0
	s_nop 0
	s_nop 0
	s_nop 0
	s_nop 0
	s_nop 0
	s_nop 0
	s_nop 0
	s_nop 0
	s_nop 0
	s_nop 0
	s_nop 0
	s_nop 0
	s_nop 0
	s_nop 0
	s_nop 0
	s_nop 0
	s_nop 0
	s_nop 0
	s_nop 0
	s_nop 0
	s_nop 0
	s_nop 0
	s_nop 0
	s_nop 0
	s_nop 0
	s_nop 0
	s_nop 0
	s_nop 0
	s_nop 0
	s_nop 0
	s_nop 0
	s_nop 0
	s_nop 0
	v_readlane_b32 s4, v251, 10
	v_readlane_b32 s6, v251, 12
	v_readlane_b32 s7, v251, 13
	s_add_u32 s30, s6, 0x100000
	s_addc_u32 s31, s7, 0
	v_readlane_b32 s5, v251, 11
	s_add_u32 s36, s6, 0x4100000
	v_readlane_b32 s0, v251, 0
	s_addc_u32 s37, s7, 0
	s_not_b32 s0, s0
	v_readlane_b32 s4, v251, 19
	s_add_i32 s47, s4, s0
	v_readlane_b32 s1, v251, 1
	s_cmpk_lt_i32 s47, 0x200
	s_cselect_b64 s[0:1], -1, 0
	s_cmpk_gt_i32 s47, 0x1ff
	v_readlane_b32 s5, v251, 20
	v_mbcnt_lo_u32_b32 v8, -1, 0
	v_mbcnt_hi_u32_b32 v8, -1, v8
	s_cbranch_scc1 .LBB0_494
	s_ashr_i32 s4, s47, 31
	s_lshr_b32 s4, s4, 29
	s_add_i32 s8, s47, s4
	s_and_b32 s4, s8, -8
	s_sub_i32 s6, s47, s4
	s_cmp_gt_i32 s6, -1
	s_cbranch_scc0 .LBB0_495
	s_lshl_b32 s7, s6, 6
	s_ashr_i32 s4, s8, 3
	s_cbranch_execz .LBB0_496
	s_branch .LBB0_497
